# strategy 1 (counted waits): MoE quantise phase Q2 - the per-row scale load no longer blocks the row loads (vmcnt(0) removed, division after the loads are in flight)
# speedup vs baseline: 1.0036x; 1.0036x over previous
.LBB0_1945:
	v_readlane_b32 s4, v253, 57
	v_ashrrev_i32_e32 v43, 31, v42
	v_readlane_b32 s5, v253, 58
	s_movk_i32 s3, 0x2c00
	v_lshlrev_b32_e32 v98, 1, v44
	v_lshl_add_u64 v[60:61], v[42:43], 2, s[4:5]
	global_load_dword v70, v[60:61], off
	v_readlane_b32 s4, v254, 13
	v_readlane_b32 s5, v254, 14
	v_mov_b32_e32 v53, v99
	v_mov_b32_e32 v55, v99
	v_mov_b32_e32 v57, v99
	v_mov_b32_e32 v59, v99
	v_mov_b64_e32 v[2:3], s[4:5]
	v_mad_i64_i32 v[2:3], s[4:5], v42, s3, v[2:3]
	v_lshl_add_u64 v[4:5], v[2:3], 0, v[98:99]
	global_load_dwordx4 v[64:67], v[4:5], off
	global_load_dwordx4 v[38:41], v[4:5], off offset:1024
	global_load_dwordx4 v[34:37], v[4:5], off offset:2048
	global_load_dwordx4 v[30:33], v[4:5], off offset:3072
	v_lshl_add_u64 v[4:5], v[2:3], 0, v[52:53]
	global_load_dwordx4 v[26:29], v[4:5], off
	v_lshl_add_u64 v[4:5], v[2:3], 0, v[54:55]
	global_load_dwordx4 v[22:25], v[4:5], off
	v_lshl_add_u64 v[4:5], v[2:3], 0, v[56:57]
	global_load_dwordx4 v[18:21], v[4:5], off
	v_lshl_add_u64 v[4:5], v[2:3], 0, v[58:59]
	v_lshlrev_b32_e32 v98, 1, v46
	global_load_dwordx4 v[14:17], v[4:5], off
	v_lshl_add_u64 v[4:5], v[2:3], 0, v[98:99]
	v_lshlrev_b32_e32 v98, 1, v48
	v_mov_b64_e32 v[62:63], s[18:19]
	s_movk_i32 s3, 0x1600
	global_load_dwordx4 v[10:13], v[4:5], off
	v_lshl_add_u64 v[4:5], v[2:3], 0, v[98:99]
	v_lshlrev_b32_e32 v98, 1, v50
	v_mad_i64_i32 v[62:63], s[4:5], v42, s3, v[62:63]
	v_lshl_add_u64 v[2:3], v[2:3], 0, v[98:99]
	global_load_dwordx4 v[6:9], v[4:5], off
	s_waitcnt vmcnt(9)
	s_mov_b32 s3, 0x42fe0000
	v_max_f32_e32 v70, v70, v70
	v_max_f32_e32 v43, 0x1e3ce508, v70
	v_div_scale_f32 v53, s[4:5], v43, v43, s3
	v_div_scale_f32 v57, vcc, s3, v43, s3
	v_rcp_f32_e32 v55, v53
	s_nop 0
	v_fma_f32 v68, -v53, v55, 1.0
	v_fmac_f32_e32 v55, v68, v55
	v_mul_f32_e32 v59, v57, v55
	v_fma_f32 v68, -v53, v59, v57
	v_fmac_f32_e32 v59, v68, v55
	v_fma_f32 v53, -v53, v59, v57
	v_div_fmas_f32 v53, v53, v55, v59
	v_div_fixup_f32 v53, v53, v43, s3
	v_lshlrev_b32_e32 v55, 16, v64
	v_and_b32_e32 v57, 0xffff0000, v64
	v_lshlrev_b32_e32 v59, 16, v65
	v_and_b32_e32 v64, 0xffff0000, v65
	v_lshlrev_b32_e32 v65, 16, v66
	v_and_b32_e32 v66, 0xffff0000, v66
	v_mul_f32_e32 v66, v53, v66
	v_rndne_f32_e32 v66, v66
	v_cvt_i32_f32_e32 v66, v66
	v_mul_f32_e32 v57, v53, v57
	v_lshlrev_b32_e32 v68, 16, v67
	v_mul_f32_e32 v55, v53, v55
	v_rndne_f32_e32 v57, v57
	v_lshlrev_b32_e32 v66, 8, v66
	v_mul_f32_e32 v59, v53, v59
	v_mul_f32_e32 v64, v53, v64
	v_rndne_f32_e32 v55, v55
	v_cvt_i32_f32_e32 v57, v57
	v_and_b32_e32 v69, 0xff00, v66
	v_rndne_f32_e32 v59, v59
	v_mul_f32_e32 v66, v53, v68
	v_rndne_f32_e32 v64, v64
	v_cvt_i32_f32_e32 v55, v55
	v_cvt_i32_f32_sdwa v59, v59 dst_sel:WORD_1 dst_unused:UNUSED_PAD src0_sel:DWORD
	v_rndne_f32_e32 v66, v66
	v_cvt_i32_f32_e32 v64, v64
	v_cvt_i32_f32_sdwa v66, v66 dst_sel:WORD_1 dst_unused:UNUSED_PAD src0_sel:DWORD
	v_lshlrev_b32_e32 v57, 8, v57
	v_and_b32_e32 v67, 0xffff0000, v67
	v_and_b32_e32 v57, 0xff00, v57
	v_and_b32_e32 v59, 0xff0000, v59
	v_perm_b32 v55, v64, v55, s7
	v_mul_f32_e32 v65, v53, v65
	v_and_b32_e32 v68, 0xff0000, v66
	v_or3_b32 v66, v55, v57, v59
	v_mul_f32_e32 v55, v53, v67
	v_rndne_f32_e32 v65, v65
	v_rndne_f32_e32 v55, v55
	v_cvt_i32_f32_e32 v65, v65
	v_cvt_i32_f32_e32 v55, v55
	s_waitcnt vmcnt(8)
	v_lshlrev_b32_e32 v57, 16, v39
	v_and_b32_e32 v39, 0xffff0000, v39
	v_mul_f32_e32 v57, v53, v57
	v_perm_b32 v55, v55, v65, s7
	v_or3_b32 v67, v55, v69, v68
	v_lshlrev_b32_e32 v55, 16, v38
	v_and_b32_e32 v38, 0xffff0000, v38
	v_mul_f32_e32 v38, v53, v38
	v_mul_f32_e32 v55, v53, v55
	v_rndne_f32_e32 v38, v38
	v_mul_f32_e32 v39, v53, v39
	v_rndne_f32_e32 v55, v55
	v_cvt_i32_f32_e32 v38, v38
	v_rndne_f32_e32 v57, v57
	v_rndne_f32_e32 v39, v39
	v_cvt_i32_f32_e32 v55, v55
	v_cvt_i32_f32_sdwa v57, v57 dst_sel:WORD_1 dst_unused:UNUSED_PAD src0_sel:DWORD
	v_cvt_i32_f32_e32 v39, v39
	v_lshl_add_u64 v[64:65], v[62:63], 0, v[44:45]
	v_lshlrev_b32_e32 v59, 16, v40
	v_and_b32_e32 v40, 0xffff0000, v40
	v_lshlrev_b32_e32 v38, 8, v38
	global_load_dwordx4 v[2:5], v[2:3], off
	v_and_b32_e32 v38, 0xff00, v38
	global_store_dwordx2 v[64:65], v[66:67], off
	v_lshlrev_b32_e32 v66, 16, v41
	v_and_b32_e32 v41, 0xffff0000, v41
	v_mul_f32_e32 v40, v53, v40
	v_and_b32_e32 v57, 0xff0000, v57
	v_perm_b32 v39, v39, v55, s7
	v_mul_f32_e32 v59, v53, v59
	v_rndne_f32_e32 v40, v40
	v_mul_f32_e32 v66, v53, v66
	v_or3_b32 v38, v39, v38, v57
	v_mul_f32_e32 v39, v53, v41
	v_rndne_f32_e32 v59, v59
	v_cvt_i32_f32_e32 v40, v40
	v_rndne_f32_e32 v66, v66
	v_rndne_f32_e32 v39, v39
	v_cvt_i32_f32_e32 v59, v59
	v_cvt_i32_f32_sdwa v66, v66 dst_sel:WORD_1 dst_unused:UNUSED_PAD src0_sel:DWORD
	v_cvt_i32_f32_e32 v39, v39
	v_lshlrev_b32_e32 v40, 8, v40
	v_and_b32_e32 v40, 0xff00, v40
	v_and_b32_e32 v66, 0xff0000, v66
	v_perm_b32 v39, v39, v59, s7
	v_or3_b32 v39, v39, v40, v66
	global_store_dwordx2 v[64:65], v[38:39], off offset:512
	s_waitcnt vmcnt(10)
	v_lshlrev_b32_e32 v38, 16, v34
	v_and_b32_e32 v34, 0xffff0000, v34
	v_lshlrev_b32_e32 v39, 16, v35
	v_and_b32_e32 v35, 0xffff0000, v35
	v_mul_f32_e32 v34, v53, v34
	v_mul_f32_e32 v38, v53, v38
	v_rndne_f32_e32 v34, v34
	v_mul_f32_e32 v39, v53, v39
	v_mul_f32_e32 v35, v53, v35
	v_rndne_f32_e32 v38, v38
	v_cvt_i32_f32_e32 v34, v34
	v_rndne_f32_e32 v39, v39
	v_rndne_f32_e32 v35, v35
	v_cvt_i32_f32_e32 v38, v38
	v_cvt_i32_f32_sdwa v39, v39 dst_sel:WORD_1 dst_unused:UNUSED_PAD src0_sel:DWORD
	v_cvt_i32_f32_e32 v35, v35
	v_lshlrev_b32_e32 v40, 16, v36
	v_and_b32_e32 v36, 0xffff0000, v36
	v_lshlrev_b32_e32 v34, 8, v34
	v_lshlrev_b32_e32 v41, 16, v37
	v_and_b32_e32 v37, 0xffff0000, v37
	v_and_b32_e32 v34, 0xff00, v34
	v_mul_f32_e32 v36, v53, v36
	v_and_b32_e32 v39, 0xff0000, v39
	v_perm_b32 v35, v35, v38, s7
	v_mul_f32_e32 v40, v53, v40
	v_rndne_f32_e32 v36, v36
	v_mul_f32_e32 v41, v53, v41
	v_or3_b32 v34, v35, v34, v39
	v_mul_f32_e32 v35, v53, v37
	v_rndne_f32_e32 v40, v40
	v_cvt_i32_f32_e32 v36, v36
	v_rndne_f32_e32 v41, v41
	v_rndne_f32_e32 v35, v35
	v_cvt_i32_f32_e32 v40, v40
	v_cvt_i32_f32_sdwa v41, v41 dst_sel:WORD_1 dst_unused:UNUSED_PAD src0_sel:DWORD
	v_cvt_i32_f32_e32 v35, v35
	v_lshlrev_b32_e32 v36, 8, v36
	v_and_b32_e32 v36, 0xff00, v36
	v_and_b32_e32 v41, 0xff0000, v41
	v_perm_b32 v35, v35, v40, s7
	v_or3_b32 v35, v35, v36, v41
	global_store_dwordx2 v[64:65], v[34:35], off offset:1024
	s_waitcnt vmcnt(10)
	v_lshlrev_b32_e32 v34, 16, v30
	v_and_b32_e32 v30, 0xffff0000, v30
	v_lshlrev_b32_e32 v35, 16, v31
	v_and_b32_e32 v31, 0xffff0000, v31
	v_mul_f32_e32 v30, v53, v30
	v_mul_f32_e32 v34, v53, v34
	v_rndne_f32_e32 v30, v30
	v_mul_f32_e32 v35, v53, v35
	v_mul_f32_e32 v31, v53, v31
	v_rndne_f32_e32 v34, v34
	v_cvt_i32_f32_e32 v30, v30
	v_rndne_f32_e32 v35, v35
	v_rndne_f32_e32 v31, v31
	v_cvt_i32_f32_e32 v34, v34
	v_cvt_i32_f32_sdwa v35, v35 dst_sel:WORD_1 dst_unused:UNUSED_PAD src0_sel:DWORD
	v_cvt_i32_f32_e32 v31, v31
	v_lshlrev_b32_e32 v36, 16, v32
	v_and_b32_e32 v32, 0xffff0000, v32
	v_lshlrev_b32_e32 v30, 8, v30
	v_lshlrev_b32_e32 v37, 16, v33
	v_and_b32_e32 v33, 0xffff0000, v33
	v_and_b32_e32 v30, 0xff00, v30
	v_mul_f32_e32 v32, v53, v32
	v_and_b32_e32 v35, 0xff0000, v35
	v_perm_b32 v31, v31, v34, s7
	v_mul_f32_e32 v36, v53, v36
	v_rndne_f32_e32 v32, v32
	v_mul_f32_e32 v37, v53, v37
	v_or3_b32 v30, v31, v30, v35
	v_mul_f32_e32 v31, v53, v33
	v_rndne_f32_e32 v36, v36
	v_cvt_i32_f32_e32 v32, v32
	v_rndne_f32_e32 v37, v37
	v_rndne_f32_e32 v31, v31
	v_cvt_i32_f32_e32 v36, v36
	v_cvt_i32_f32_sdwa v37, v37 dst_sel:WORD_1 dst_unused:UNUSED_PAD src0_sel:DWORD
	v_cvt_i32_f32_e32 v31, v31
	v_lshlrev_b32_e32 v32, 8, v32
	v_and_b32_e32 v32, 0xff00, v32
	v_and_b32_e32 v37, 0xff0000, v37
	v_perm_b32 v31, v31, v36, s7
	v_or3_b32 v31, v31, v32, v37
	global_store_dwordx2 v[64:65], v[30:31], off offset:1536
	s_waitcnt vmcnt(10)
	v_lshlrev_b32_e32 v30, 16, v26
	v_and_b32_e32 v26, 0xffff0000, v26
	v_lshlrev_b32_e32 v31, 16, v27
	v_and_b32_e32 v27, 0xffff0000, v27
	v_mul_f32_e32 v26, v53, v26
	v_mul_f32_e32 v30, v53, v30
	v_rndne_f32_e32 v26, v26
	v_mul_f32_e32 v31, v53, v31
	v_mul_f32_e32 v27, v53, v27
	v_rndne_f32_e32 v30, v30
	v_cvt_i32_f32_e32 v26, v26
	v_rndne_f32_e32 v31, v31
	v_rndne_f32_e32 v27, v27
	v_cvt_i32_f32_e32 v30, v30
	v_cvt_i32_f32_sdwa v31, v31 dst_sel:WORD_1 dst_unused:UNUSED_PAD src0_sel:DWORD
	v_cvt_i32_f32_e32 v27, v27
	v_lshlrev_b32_e32 v32, 16, v28
	v_and_b32_e32 v28, 0xffff0000, v28
	v_lshlrev_b32_e32 v26, 8, v26
	v_lshlrev_b32_e32 v33, 16, v29
	v_and_b32_e32 v29, 0xffff0000, v29
	v_and_b32_e32 v26, 0xff00, v26
	v_mul_f32_e32 v28, v53, v28
	v_and_b32_e32 v31, 0xff0000, v31
	v_perm_b32 v27, v27, v30, s7
	v_mul_f32_e32 v32, v53, v32
	v_rndne_f32_e32 v28, v28
	v_mul_f32_e32 v33, v53, v33
	v_or3_b32 v26, v27, v26, v31
	v_mul_f32_e32 v27, v53, v29
	v_rndne_f32_e32 v32, v32
	v_cvt_i32_f32_e32 v28, v28
	v_rndne_f32_e32 v33, v33
	v_rndne_f32_e32 v27, v27
	v_cvt_i32_f32_e32 v32, v32
	v_cvt_i32_f32_sdwa v33, v33 dst_sel:WORD_1 dst_unused:UNUSED_PAD src0_sel:DWORD
	v_cvt_i32_f32_e32 v27, v27
	v_lshlrev_b32_e32 v28, 8, v28
	v_and_b32_e32 v28, 0xff00, v28
	v_and_b32_e32 v33, 0xff0000, v33
	v_perm_b32 v27, v27, v32, s7
	v_or3_b32 v27, v27, v28, v33
	global_store_dwordx2 v[64:65], v[26:27], off offset:2048
	s_waitcnt vmcnt(10)
	v_lshlrev_b32_e32 v26, 16, v22
	v_and_b32_e32 v22, 0xffff0000, v22
	v_lshlrev_b32_e32 v27, 16, v23
	v_and_b32_e32 v23, 0xffff0000, v23
	v_mul_f32_e32 v22, v53, v22
	v_mul_f32_e32 v26, v53, v26
	v_rndne_f32_e32 v22, v22
	v_mul_f32_e32 v27, v53, v27
	v_mul_f32_e32 v23, v53, v23
	v_rndne_f32_e32 v26, v26
	v_cvt_i32_f32_e32 v22, v22
	v_rndne_f32_e32 v27, v27
	v_rndne_f32_e32 v23, v23
	v_cvt_i32_f32_e32 v26, v26
	v_cvt_i32_f32_sdwa v27, v27 dst_sel:WORD_1 dst_unused:UNUSED_PAD src0_sel:DWORD
	v_cvt_i32_f32_e32 v23, v23
	v_lshlrev_b32_e32 v28, 16, v24
	v_and_b32_e32 v24, 0xffff0000, v24
	v_lshlrev_b32_e32 v22, 8, v22
	v_lshlrev_b32_e32 v29, 16, v25
	v_and_b32_e32 v25, 0xffff0000, v25
	v_and_b32_e32 v22, 0xff00, v22
	v_mul_f32_e32 v24, v53, v24
	v_and_b32_e32 v27, 0xff0000, v27
	v_perm_b32 v23, v23, v26, s7
	v_mul_f32_e32 v28, v53, v28
	v_rndne_f32_e32 v24, v24
	v_mul_f32_e32 v29, v53, v29
	v_or3_b32 v22, v23, v22, v27
	v_mul_f32_e32 v23, v53, v25
	v_rndne_f32_e32 v28, v28
	v_cvt_i32_f32_e32 v24, v24
	v_rndne_f32_e32 v29, v29
	v_rndne_f32_e32 v23, v23
	v_cvt_i32_f32_e32 v28, v28
	v_cvt_i32_f32_sdwa v29, v29 dst_sel:WORD_1 dst_unused:UNUSED_PAD src0_sel:DWORD
	v_cvt_i32_f32_e32 v23, v23
	v_lshlrev_b32_e32 v24, 8, v24
	v_and_b32_e32 v24, 0xff00, v24
	v_and_b32_e32 v29, 0xff0000, v29
	v_perm_b32 v23, v23, v28, s7
	v_or3_b32 v23, v23, v24, v29
	global_store_dwordx2 v[64:65], v[22:23], off offset:2560
	s_waitcnt vmcnt(10)
	v_lshlrev_b32_e32 v22, 16, v18
	v_and_b32_e32 v18, 0xffff0000, v18
	v_lshlrev_b32_e32 v23, 16, v19
	v_and_b32_e32 v19, 0xffff0000, v19
	v_mul_f32_e32 v18, v53, v18
	v_mul_f32_e32 v22, v53, v22
	v_rndne_f32_e32 v18, v18
	v_mul_f32_e32 v23, v53, v23
	v_mul_f32_e32 v19, v53, v19
	v_rndne_f32_e32 v22, v22
	v_cvt_i32_f32_e32 v18, v18
	v_rndne_f32_e32 v23, v23
	v_rndne_f32_e32 v19, v19
	v_cvt_i32_f32_e32 v22, v22
	v_cvt_i32_f32_sdwa v23, v23 dst_sel:WORD_1 dst_unused:UNUSED_PAD src0_sel:DWORD
	v_cvt_i32_f32_e32 v19, v19
	v_lshlrev_b32_e32 v24, 16, v20
	v_and_b32_e32 v20, 0xffff0000, v20
	v_lshlrev_b32_e32 v18, 8, v18
	v_lshlrev_b32_e32 v25, 16, v21
	v_and_b32_e32 v21, 0xffff0000, v21
	v_and_b32_e32 v18, 0xff00, v18
	v_mul_f32_e32 v20, v53, v20
	v_and_b32_e32 v23, 0xff0000, v23
	v_perm_b32 v19, v19, v22, s7
	v_mul_f32_e32 v24, v53, v24
	v_rndne_f32_e32 v20, v20
	v_mul_f32_e32 v25, v53, v25
	v_or3_b32 v18, v19, v18, v23
	v_mul_f32_e32 v19, v53, v21
	v_rndne_f32_e32 v24, v24
	v_cvt_i32_f32_e32 v20, v20
	v_rndne_f32_e32 v25, v25
	v_rndne_f32_e32 v19, v19
	v_cvt_i32_f32_e32 v24, v24
	v_cvt_i32_f32_sdwa v25, v25 dst_sel:WORD_1 dst_unused:UNUSED_PAD src0_sel:DWORD
	v_cvt_i32_f32_e32 v19, v19
	v_lshlrev_b32_e32 v20, 8, v20
	v_and_b32_e32 v20, 0xff00, v20
	v_and_b32_e32 v25, 0xff0000, v25
	v_perm_b32 v19, v19, v24, s7
	v_or3_b32 v19, v19, v20, v25
	global_store_dwordx2 v[64:65], v[18:19], off offset:3072
	s_waitcnt vmcnt(10)
	v_lshlrev_b32_e32 v18, 16, v14
	v_and_b32_e32 v14, 0xffff0000, v14
	v_lshlrev_b32_e32 v19, 16, v15
	v_and_b32_e32 v15, 0xffff0000, v15
	v_mul_f32_e32 v14, v53, v14
	v_mul_f32_e32 v18, v53, v18
	v_rndne_f32_e32 v14, v14
	v_mul_f32_e32 v19, v53, v19
	v_mul_f32_e32 v15, v53, v15
	v_rndne_f32_e32 v18, v18
	v_cvt_i32_f32_e32 v14, v14
	v_rndne_f32_e32 v19, v19
	v_rndne_f32_e32 v15, v15
	v_cvt_i32_f32_e32 v18, v18
	v_cvt_i32_f32_sdwa v19, v19 dst_sel:WORD_1 dst_unused:UNUSED_PAD src0_sel:DWORD
	v_cvt_i32_f32_e32 v15, v15
	v_lshlrev_b32_e32 v20, 16, v16
	v_and_b32_e32 v16, 0xffff0000, v16
	v_lshlrev_b32_e32 v14, 8, v14
	v_lshlrev_b32_e32 v21, 16, v17
	v_and_b32_e32 v17, 0xffff0000, v17
	v_and_b32_e32 v14, 0xff00, v14
	v_mul_f32_e32 v16, v53, v16
	v_and_b32_e32 v19, 0xff0000, v19
	v_perm_b32 v15, v15, v18, s7
	v_mul_f32_e32 v20, v53, v20
	v_rndne_f32_e32 v16, v16
	v_mul_f32_e32 v21, v53, v21
	v_or3_b32 v14, v15, v14, v19
	v_mul_f32_e32 v15, v53, v17
	v_rndne_f32_e32 v20, v20
	v_cvt_i32_f32_e32 v16, v16
	v_rndne_f32_e32 v21, v21
	v_rndne_f32_e32 v15, v15
	v_cvt_i32_f32_e32 v20, v20
	v_cvt_i32_f32_sdwa v21, v21 dst_sel:WORD_1 dst_unused:UNUSED_PAD src0_sel:DWORD
	v_cvt_i32_f32_e32 v15, v15
	v_lshlrev_b32_e32 v16, 8, v16
	v_and_b32_e32 v16, 0xff00, v16
	v_and_b32_e32 v21, 0xff0000, v21
	v_perm_b32 v15, v15, v20, s7
	v_or3_b32 v15, v15, v16, v21
	global_store_dwordx2 v[64:65], v[14:15], off offset:3584
	s_waitcnt vmcnt(10)
	v_lshlrev_b32_e32 v14, 16, v10
	v_and_b32_e32 v10, 0xffff0000, v10
	v_lshlrev_b32_e32 v15, 16, v11
	v_and_b32_e32 v11, 0xffff0000, v11
	v_mul_f32_e32 v10, v53, v10
	v_mul_f32_e32 v14, v53, v14
	v_rndne_f32_e32 v10, v10
	v_mul_f32_e32 v15, v53, v15
	v_mul_f32_e32 v11, v53, v11
	v_rndne_f32_e32 v14, v14
	v_cvt_i32_f32_e32 v10, v10
	v_rndne_f32_e32 v15, v15
	v_rndne_f32_e32 v11, v11
	v_cvt_i32_f32_e32 v14, v14
	v_cvt_i32_f32_sdwa v15, v15 dst_sel:WORD_1 dst_unused:UNUSED_PAD src0_sel:DWORD
	v_cvt_i32_f32_e32 v11, v11
	v_lshlrev_b32_e32 v16, 16, v12
	v_and_b32_e32 v12, 0xffff0000, v12
	v_lshlrev_b32_e32 v10, 8, v10
	v_lshlrev_b32_e32 v17, 16, v13
	v_and_b32_e32 v13, 0xffff0000, v13
	v_and_b32_e32 v10, 0xff00, v10
	v_mul_f32_e32 v12, v53, v12
	v_and_b32_e32 v15, 0xff0000, v15
	v_perm_b32 v11, v11, v14, s7
	v_mul_f32_e32 v16, v53, v16
	v_rndne_f32_e32 v12, v12
	v_mul_f32_e32 v17, v53, v17
	v_or3_b32 v10, v11, v10, v15
	v_mul_f32_e32 v11, v53, v13
	v_rndne_f32_e32 v16, v16
	v_cvt_i32_f32_e32 v12, v12
	v_rndne_f32_e32 v17, v17
	v_rndne_f32_e32 v11, v11
	v_cvt_i32_f32_e32 v16, v16
	v_cvt_i32_f32_sdwa v17, v17 dst_sel:WORD_1 dst_unused:UNUSED_PAD src0_sel:DWORD
	v_cvt_i32_f32_e32 v11, v11
	v_lshlrev_b32_e32 v12, 8, v12
	v_and_b32_e32 v12, 0xff00, v12
	v_and_b32_e32 v17, 0xff0000, v17
	v_perm_b32 v11, v11, v16, s7
	v_or3_b32 v11, v11, v12, v17
	v_lshl_add_u64 v[12:13], v[62:63], 0, v[46:47]
	global_store_dwordx2 v[12:13], v[10:11], off
	s_waitcnt vmcnt(10)
	v_lshlrev_b32_e32 v10, 16, v6
	v_and_b32_e32 v6, 0xffff0000, v6
	v_lshlrev_b32_e32 v11, 16, v7
	v_and_b32_e32 v7, 0xffff0000, v7
	v_mul_f32_e32 v6, v53, v6
	v_mul_f32_e32 v10, v53, v10
	v_rndne_f32_e32 v6, v6
	v_mul_f32_e32 v11, v53, v11
	v_mul_f32_e32 v7, v53, v7
	v_rndne_f32_e32 v10, v10
	v_cvt_i32_f32_e32 v6, v6
	v_rndne_f32_e32 v11, v11
	v_rndne_f32_e32 v7, v7
	v_cvt_i32_f32_e32 v10, v10
	v_cvt_i32_f32_sdwa v11, v11 dst_sel:WORD_1 dst_unused:UNUSED_PAD src0_sel:DWORD
	v_cvt_i32_f32_e32 v7, v7
	v_lshlrev_b32_e32 v12, 16, v8
	v_and_b32_e32 v8, 0xffff0000, v8
	v_lshlrev_b32_e32 v6, 8, v6
	v_lshlrev_b32_e32 v13, 16, v9
	v_and_b32_e32 v9, 0xffff0000, v9
	v_and_b32_e32 v6, 0xff00, v6
	v_mul_f32_e32 v8, v53, v8
	v_and_b32_e32 v11, 0xff0000, v11
	v_perm_b32 v7, v7, v10, s7
	v_mul_f32_e32 v12, v53, v12
	v_rndne_f32_e32 v8, v8
	v_mul_f32_e32 v13, v53, v13
	v_or3_b32 v6, v7, v6, v11
	v_mul_f32_e32 v7, v53, v9
	v_rndne_f32_e32 v12, v12
	v_cvt_i32_f32_e32 v8, v8
	v_rndne_f32_e32 v13, v13
	v_rndne_f32_e32 v7, v7
	v_cvt_i32_f32_e32 v12, v12
	v_cvt_i32_f32_sdwa v13, v13 dst_sel:WORD_1 dst_unused:UNUSED_PAD src0_sel:DWORD
	v_cvt_i32_f32_e32 v7, v7
	v_lshlrev_b32_e32 v8, 8, v8
	v_and_b32_e32 v8, 0xff00, v8
	v_and_b32_e32 v13, 0xff0000, v13
	v_perm_b32 v7, v7, v12, s7
	v_or3_b32 v7, v7, v8, v13
	v_lshl_add_u64 v[8:9], v[62:63], 0, v[48:49]
	global_store_dwordx2 v[8:9], v[6:7], off
	s_waitcnt vmcnt(10)
	v_lshlrev_b32_e32 v6, 16, v2
	v_and_b32_e32 v2, 0xffff0000, v2
	v_lshlrev_b32_e32 v7, 16, v3
	v_and_b32_e32 v3, 0xffff0000, v3
	v_mul_f32_e32 v2, v53, v2
	v_mul_f32_e32 v6, v53, v6
	v_rndne_f32_e32 v2, v2
	v_mul_f32_e32 v7, v53, v7
	v_mul_f32_e32 v3, v53, v3
	v_rndne_f32_e32 v6, v6
	v_cvt_i32_f32_e32 v2, v2
	v_rndne_f32_e32 v7, v7
	v_rndne_f32_e32 v3, v3
	v_cvt_i32_f32_e32 v6, v6
	v_cvt_i32_f32_sdwa v7, v7 dst_sel:WORD_1 dst_unused:UNUSED_PAD src0_sel:DWORD
	v_cvt_i32_f32_e32 v3, v3
	v_lshlrev_b32_e32 v8, 16, v4
	v_and_b32_e32 v4, 0xffff0000, v4
	v_lshlrev_b32_e32 v2, 8, v2
	v_lshlrev_b32_e32 v9, 16, v5
	v_and_b32_e32 v5, 0xffff0000, v5
	v_and_b32_e32 v2, 0xff00, v2
	v_mul_f32_e32 v4, v53, v4
	v_and_b32_e32 v7, 0xff0000, v7
	v_perm_b32 v3, v3, v6, s7
	v_mul_f32_e32 v8, v53, v8
	v_rndne_f32_e32 v4, v4
	v_mul_f32_e32 v9, v53, v9
	v_or3_b32 v2, v3, v2, v7
	v_mul_f32_e32 v3, v53, v5
	v_rndne_f32_e32 v8, v8
	v_cvt_i32_f32_e32 v4, v4
	v_rndne_f32_e32 v9, v9
	v_rndne_f32_e32 v3, v3
	v_cvt_i32_f32_e32 v8, v8
	v_cvt_i32_f32_sdwa v9, v9 dst_sel:WORD_1 dst_unused:UNUSED_PAD src0_sel:DWORD
	v_cvt_i32_f32_e32 v3, v3
	v_lshlrev_b32_e32 v4, 8, v4
	v_and_b32_e32 v4, 0xff00, v4
	v_and_b32_e32 v9, 0xff0000, v9
	v_perm_b32 v3, v3, v8, s7
	v_or3_b32 v3, v3, v4, v9
	v_lshl_add_u64 v[4:5], v[62:63], 0, v[50:51]
	global_store_dwordx2 v[4:5], v[2:3], off
	s_and_saveexec_b64 s[4:5], s[0:1]
	s_cbranch_execz .LBB0_1944
	v_mul_f32_e32 v2, 0x3c010204, v43
	global_store_dword v[60:61], v2, off
	s_branch .LBB0_1944
